# pj K-loop: trailing s_barrier of each MFMA section moved up 4 MFMAs
# speedup vs baseline: 1.0027x; 1.0027x over previous
; #define PG8_STAGE(bufoff, gbase, voff) do { _Pragma("unroll") for (int _i = 0; _i < 2; ++_i) \
;         __builtin_amdgcn_global_load_lds((const unsigned*)((const char*)(gbase) + (voff)[_i]), (LAS unsigned*)(lds + (bufoff) + ldsw + _i * 8192), 16, 0, 0); } while (0)
; #define PG8_LDA(dst, b, h) do { _Pragma("unroll") for (int m = 0; m < 4; ++m) _Pragma("unroll") for (int k = 0; k < 2; ++k) dst[m][k] = *(const LAS bf16x8*)(lds + PG8_SA(b, h) + aoff + m * 2048 + k * 1024); } while (0)
; #define PG8_LDB(dst, b, h) do { _Pragma("unroll") for (int n = 0; n < 2; ++n) _Pragma("unroll") for (int k = 0; k < 2; ++k) dst[n][k] = *(const LAS bf16x8*)(lds + PG8_SB(b, h) + boff + n * 2048 + k * 1024); } while (0)
; #define PG8_MMA(ai, bj, At, Bt) do { __builtin_amdgcn_s_setprio(1); _Pragma("unroll") for (int m = 0; m < 4; ++m) _Pragma("unroll") for (int n = 0; n < 2; ++n) _Pragma("unroll") for (int k = 0; k < 2; ++k) \
;         acc[ai][bj][m][n] = __builtin_amdgcn_mfma_f32_16x16x32_bf16(Bt[n][k], At[m][k], acc[ai][bj][m][n], 0, 0, 0); __builtin_amdgcn_s_setprio(0); } while (0)
; #define PG8_WAIT_V(n) asm volatile("s_waitcnt vmcnt(" #n ")" ::: "memory")
; #define PG8_WAIT_L(n) asm volatile("s_waitcnt lgkmcnt(" #n ")" ::: "memory")
; #define PG8_BAR __builtin_amdgcn_s_barrier()
; #define PG8_SCHED __builtin_amdgcn_sched_barrier(0)
; #define PG8_STAGE(bufoff, gbase, voff) do { _Pragma("unroll") for (int _i = 0; _i < 2; ++_i) \
;         __builtin_amdgcn_global_load_lds((const unsigned*)((const char*)(gbase) + (voff)[_i]), (LAS unsigned*)(lds + (bufoff) + ldsw + _i * 8192), 16, 0, 0); } while (0)
; #define PG8_LDA(dst, b, h) do { _Pragma("unroll") for (int m = 0; m < 4; ++m) _Pragma("unroll") for (int k = 0; k < 2; ++k) dst[m][k] = *(const LAS bf16x8*)(lds + PG8_SA(b, h) + aoff + m * 2048 + k * 1024); } while (0)
;     ...
;             PG8_LDB(B0, 0, 0); PG8_LDB(B1, 0, 1); PG8_SCHED; PG8_LDA(At, 0, 0); PG8_STAGE(PG8_SA(1, 1), a1 + hstepA, voffA);
;             PG8_WAIT_V(8); PG8_WAIT_L(0); PG8_BAR; PG8_MMA(0, 0, At, B0); PG8_MMA(0, 1, At, B1); PG8_BAR; PG8_SCHED;
;             PG8_LDA(At, 0, 1); PG8_STAGE(PG8_SB(0, 0), b2, voffB); PG8_STAGE(PG8_SB(0, 1), b2 + hstep, voffB); PG8_STAGE(PG8_SA(0, 0), a2, voffA);
;             PG8_WAIT_V(8); PG8_WAIT_L(0); PG8_BAR; if (hi_on) { PG8_MMA(1, 0, At, B0); PG8_MMA(1, 1, At, B1); } PG8_BAR; PG8_SCHED;
.LBB0_213:
	s_add_u32 s22, s6, 0xfffc0080
	s_addc_u32 s23, s7, -1
	s_add_i32 s27, 0, 0x10000
	s_cmp_eq_u32 s26, 12
	s_cselect_b32 s25, s19, s23
	s_cselect_b32 s24, s18, s22
	v_add_u32_e32 v52, s27, v1
	s_cselect_b32 s23, s21, s17
	s_cselect_b32 s22, s20, s15
	s_add_i32 s42, 0, 0x14000
	ds_read_b128 v[62:65], v52
	ds_read_b128 v[66:69], v52 offset:1024
	ds_read_b128 v[156:159], v52 offset:2048
	ds_read_b128 v[160:163], v52 offset:3072
	v_add_u32_e32 v52, s42, v1
	ds_read_b128 v[168:171], v52
	ds_read_b128 v[172:175], v52 offset:1024
	ds_read_b128 v[176:179], v52 offset:2048
	ds_read_b128 v[180:183], v52 offset:3072
	v_lshl_add_u64 v[52:53], s[6:7], 0, v[152:153]
	s_add_i32 m0, s30, 0xc000
	ds_read_b128 v[184:187], v166
	ds_read_b128 v[188:191], v166 offset:1024
	ds_read_b128 v[192:195], v166 offset:2048
	ds_read_b128 v[204:207], v166 offset:3072
	ds_read_b128 v[208:211], v166 offset:4096
	ds_read_b128 v[212:215], v166 offset:5120
	ds_read_b128 v[216:219], v166 offset:6144
	ds_read_b128 v[220:223], v166 offset:7168
	global_load_lds_dwordx4 v[52:53], off
	v_lshl_add_u64 v[52:53], s[6:7], 0, v[154:155]
	s_add_i32 m0, s30, 0xe000
	s_nop 0
	global_load_lds_dwordx4 v[52:53], off
	s_waitcnt vmcnt(8)
	s_waitcnt lgkmcnt(0)
	s_barrier
	s_setprio 1
	s_waitcnt lgkmcnt(0)
	v_mfma_f32_16x16x32_bf16 v[138:141], v[62:65], v[184:187], v[138:141]
	v_mfma_f32_16x16x32_bf16 v[134:137], v[156:159], v[184:187], v[134:137]
	v_mfma_f32_16x16x32_bf16 v[122:125], v[62:65], v[192:195], v[122:125]
	v_mfma_f32_16x16x32_bf16 v[118:121], v[156:159], v[192:195], v[118:121]
	v_mfma_f32_16x16x32_bf16 v[106:109], v[62:65], v[208:211], v[106:109]
	v_mfma_f32_16x16x32_bf16 v[102:105], v[156:159], v[208:211], v[102:105]
	v_mfma_f32_16x16x32_bf16 v[90:93], v[62:65], v[216:219], v[90:93]
	v_mfma_f32_16x16x32_bf16 v[86:89], v[156:159], v[216:219], v[86:89]
	v_mfma_f32_16x16x32_bf16 v[138:141], v[66:69], v[188:191], v[138:141]
	v_mfma_f32_16x16x32_bf16 v[134:137], v[160:163], v[188:191], v[134:137]
	v_mfma_f32_16x16x32_bf16 v[122:125], v[66:69], v[204:207], v[122:125]
	v_mfma_f32_16x16x32_bf16 v[118:121], v[160:163], v[204:207], v[118:121]
	v_mfma_f32_16x16x32_bf16 v[106:109], v[66:69], v[212:215], v[106:109]
	v_mfma_f32_16x16x32_bf16 v[102:105], v[160:163], v[212:215], v[102:105]
	v_mfma_f32_16x16x32_bf16 v[90:93], v[66:69], v[220:223], v[90:93]
	v_mfma_f32_16x16x32_bf16 v[86:89], v[160:163], v[220:223], v[86:89]
	s_setprio 0
	s_setprio 1
	v_mfma_f32_16x16x32_bf16 v[130:133], v[168:171], v[184:187], v[130:133]
	v_mfma_f32_16x16x32_bf16 v[126:129], v[176:179], v[184:187], v[126:129]
	v_mfma_f32_16x16x32_bf16 v[114:117], v[168:171], v[192:195], v[114:117]
	v_mfma_f32_16x16x32_bf16 v[110:113], v[176:179], v[192:195], v[110:113]
	v_mfma_f32_16x16x32_bf16 v[98:101], v[168:171], v[208:211], v[98:101]
	v_mfma_f32_16x16x32_bf16 v[94:97], v[176:179], v[208:211], v[94:97]
	v_mfma_f32_16x16x32_bf16 v[82:85], v[168:171], v[216:219], v[82:85]
	v_mfma_f32_16x16x32_bf16 v[78:81], v[176:179], v[216:219], v[78:81]
	v_mfma_f32_16x16x32_bf16 v[130:133], v[172:175], v[188:191], v[130:133]
	v_mfma_f32_16x16x32_bf16 v[126:129], v[180:183], v[188:191], v[126:129]
	v_mfma_f32_16x16x32_bf16 v[114:117], v[172:175], v[204:207], v[114:117]
	v_mfma_f32_16x16x32_bf16 v[110:113], v[180:183], v[204:207], v[110:113]
	s_barrier
	v_mfma_f32_16x16x32_bf16 v[98:101], v[172:175], v[212:215], v[98:101]
	v_mfma_f32_16x16x32_bf16 v[94:97], v[180:183], v[212:215], v[94:97]
	v_mfma_f32_16x16x32_bf16 v[82:85], v[172:175], v[220:223], v[82:85]
	v_mfma_f32_16x16x32_bf16 v[78:81], v[180:183], v[220:223], v[78:81]
	s_setprio 0
	s_add_i32 s27, s27, s29
	v_lshl_add_u64 v[196:197], s[22:23], 0, v[144:145]
	s_mov_b32 m0, s27
	ds_read_b128 v[184:187], v166 offset:16384
	ds_read_b128 v[188:191], v166 offset:17408
	ds_read_b128 v[192:195], v166 offset:18432
	ds_read_b128 v[204:207], v166 offset:19456
	ds_read_b128 v[208:211], v166 offset:20480
	ds_read_b128 v[212:215], v166 offset:21504
	ds_read_b128 v[216:219], v166 offset:22528
	ds_read_b128 v[220:223], v166 offset:23552
	global_load_lds_dwordx4 v[196:197], off
	s_add_i32 m0, s27, 0x2000
	s_add_u32 s36, s22, 0x40000
	v_lshl_add_u64 v[224:225], s[22:23], 0, v[148:149]
	s_addc_u32 s37, s23, 0
	s_add_i32 s27, s42, s29
	global_load_lds_dwordx4 v[224:225], off
	v_lshl_add_u64 v[52:53], s[36:37], 0, v[144:145]
	s_mov_b32 m0, s27
	v_lshl_add_u64 v[226:227], s[24:25], 0, v[142:143]
	global_load_lds_dwordx4 v[52:53], off
	v_lshl_add_u64 v[52:53], s[36:37], 0, v[148:149]
	s_add_i32 m0, s27, 0x2000
	v_lshl_add_u64 v[228:229], s[24:25], 0, v[146:147]
	global_load_lds_dwordx4 v[52:53], off
	s_mov_b32 m0, s30
	s_nop 0
	global_load_lds_dwordx4 v[226:227], off
	s_mov_b32 m0, s31
	s_nop 0
	global_load_lds_dwordx4 v[228:229], off
	s_waitcnt vmcnt(8)
	s_waitcnt lgkmcnt(0)
	s_barrier
; #define PG8_STAGE(bufoff, gbase, voff) do { _Pragma("unroll") for (int _i = 0; _i < 2; ++_i) \
;         __builtin_amdgcn_global_load_lds((const unsigned*)((const char*)(gbase) + (voff)[_i]), (LAS unsigned*)(lds + (bufoff) + ldsw + _i * 8192), 16, 0, 0); } while (0)
; #define PG8_LDA(dst, b, h) do { _Pragma("unroll") for (int m = 0; m < 4; ++m) _Pragma("unroll") for (int k = 0; k < 2; ++k) dst[m][k] = *(const LAS bf16x8*)(lds + PG8_SA(b, h) + aoff + m * 2048 + k * 1024); } while (0)
; #define PG8_LDB(dst, b, h) do { _Pragma("unroll") for (int n = 0; n < 2; ++n) _Pragma("unroll") for (int k = 0; k < 2; ++k) dst[n][k] = *(const LAS bf16x8*)(lds + PG8_SB(b, h) + boff + n * 2048 + k * 1024); } while (0)
; #define PG8_MMA(ai, bj, At, Bt) do { __builtin_amdgcn_s_setprio(1); _Pragma("unroll") for (int m = 0; m < 4; ++m) _Pragma("unroll") for (int n = 0; n < 2; ++n) _Pragma("unroll") for (int k = 0; k < 2; ++k) \
;         acc[ai][bj][m][n] = __builtin_amdgcn_mfma_f32_16x16x32_bf16(Bt[n][k], At[m][k], acc[ai][bj][m][n], 0, 0, 0); __builtin_amdgcn_s_setprio(0); } while (0)
; #define PG8_WAIT_V(n) asm volatile("s_waitcnt vmcnt(" #n ")" ::: "memory")
; #define PG8_WAIT_L(n) asm volatile("s_waitcnt lgkmcnt(" #n ")" ::: "memory")
; #define PG8_BAR __builtin_amdgcn_s_barrier()
; #define PG8_SCHED __builtin_amdgcn_sched_barrier(0)
; #define PG8_STAGE(bufoff, gbase, voff) do { _Pragma("unroll") for (int _i = 0; _i < 2; ++_i) \
;         __builtin_amdgcn_global_load_lds((const unsigned*)((const char*)(gbase) + (voff)[_i]), (LAS unsigned*)(lds + (bufoff) + ldsw + _i * 8192), 16, 0, 0); } while (0)
; #define PG8_LDA(dst, b, h) do { _Pragma("unroll") for (int m = 0; m < 4; ++m) _Pragma("unroll") for (int k = 0; k < 2; ++k) dst[m][k] = *(const LAS bf16x8*)(lds + PG8_SA(b, h) + aoff + m * 2048 + k * 1024); } while (0)
; #define PG8_WAIT_V(n) asm volatile("s_waitcnt vmcnt(" #n ")" ::: "memory")
; #define PG8_WAIT_L(n) asm volatile("s_waitcnt lgkmcnt(" #n ")" ::: "memory")
;     ...
;             PG8_WAIT_V(8); PG8_WAIT_L(0); PG8_BAR; if (hi_on) { PG8_MMA(1, 0, At, B0); PG8_MMA(1, 1, At, B1); } PG8_BAR; PG8_SCHED;
;             PG8_LDB(B0, 1, 0); PG8_LDB(B1, 1, 1); PG8_SCHED; PG8_LDA(At, 1, 0); PG8_STAGE(PG8_SA(0, 1), a2 + hstepA, voffA);
;             PG8_WAIT_V(8); PG8_WAIT_L(0); PG8_BAR; PG8_MMA(0, 0, At, B0); PG8_MMA(0, 1, At, B1); PG8_BAR; PG8_SCHED;
	s_setprio 1
	s_waitcnt lgkmcnt(0)
	v_mfma_f32_16x16x32_bf16 v[74:77], v[62:65], v[184:187], v[74:77]
	v_mfma_f32_16x16x32_bf16 v[70:73], v[156:159], v[184:187], v[70:73]
	v_mfma_f32_16x16x32_bf16 v[48:51], v[62:65], v[192:195], v[48:51]
	v_mfma_f32_16x16x32_bf16 v[44:47], v[156:159], v[192:195], v[44:47]
	v_mfma_f32_16x16x32_bf16 v[30:33], v[62:65], v[208:211], v[30:33]
	v_mfma_f32_16x16x32_bf16 v[26:29], v[156:159], v[208:211], v[26:29]
	v_mfma_f32_16x16x32_bf16 v[14:17], v[62:65], v[216:219], v[14:17]
	v_mfma_f32_16x16x32_bf16 v[10:13], v[156:159], v[216:219], v[10:13]
	v_mfma_f32_16x16x32_bf16 v[74:77], v[66:69], v[188:191], v[74:77]
	v_mfma_f32_16x16x32_bf16 v[70:73], v[160:163], v[188:191], v[70:73]
	v_mfma_f32_16x16x32_bf16 v[48:51], v[66:69], v[204:207], v[48:51]
	v_mfma_f32_16x16x32_bf16 v[44:47], v[160:163], v[204:207], v[44:47]
	v_mfma_f32_16x16x32_bf16 v[30:33], v[66:69], v[212:215], v[30:33]
	v_mfma_f32_16x16x32_bf16 v[26:29], v[160:163], v[212:215], v[26:29]
	v_mfma_f32_16x16x32_bf16 v[14:17], v[66:69], v[220:223], v[14:17]
	v_mfma_f32_16x16x32_bf16 v[10:13], v[160:163], v[220:223], v[10:13]
	s_setprio 0
	s_setprio 1
	v_mfma_f32_16x16x32_bf16 v[58:61], v[168:171], v[184:187], v[58:61]
	v_mfma_f32_16x16x32_bf16 v[52:55], v[176:179], v[184:187], v[54:57]
	v_mfma_f32_16x16x32_bf16 v[40:43], v[168:171], v[192:195], v[40:43]
	v_mfma_f32_16x16x32_bf16 v[36:39], v[176:179], v[192:195], v[36:39]
	v_mfma_f32_16x16x32_bf16 v[22:25], v[168:171], v[208:211], v[22:25]
	v_mfma_f32_16x16x32_bf16 v[18:21], v[176:179], v[208:211], v[18:21]
	v_mfma_f32_16x16x32_bf16 v[6:9], v[168:171], v[216:219], v[6:9]
	v_mfma_f32_16x16x32_bf16 v[2:5], v[176:179], v[216:219], v[2:5]
	v_mfma_f32_16x16x32_bf16 v[58:61], v[172:175], v[188:191], v[58:61]
	v_mfma_f32_16x16x32_bf16 v[52:55], v[180:183], v[188:191], v[52:55]
	v_mfma_f32_16x16x32_bf16 v[40:43], v[172:175], v[204:207], v[40:43]
	v_mfma_f32_16x16x32_bf16 v[36:39], v[180:183], v[204:207], v[36:39]
	s_barrier
	v_mfma_f32_16x16x32_bf16 v[22:25], v[172:175], v[212:215], v[22:25]
	v_mfma_f32_16x16x32_bf16 v[18:21], v[180:183], v[212:215], v[18:21]
	v_mfma_f32_16x16x32_bf16 v[6:9], v[172:175], v[220:223], v[6:9]
	v_mfma_f32_16x16x32_bf16 v[2:5], v[180:183], v[220:223], v[2:5]
	s_setprio 0
	s_add_i32 s27, 0, 0x18000
	v_add_u32_e32 v56, s27, v1
	s_add_i32 s36, 0, 0x1c000
	ds_read_b128 v[62:65], v56
	ds_read_b128 v[66:69], v56 offset:1024
	ds_read_b128 v[156:159], v56 offset:2048
	ds_read_b128 v[160:163], v56 offset:3072
	v_add_u32_e32 v56, s36, v1
	ds_read_b128 v[168:171], v56
	ds_read_b128 v[172:175], v56 offset:1024
	ds_read_b128 v[176:179], v56 offset:2048
	ds_read_b128 v[180:183], v56 offset:3072
	s_add_u32 s24, s24, 0x40000
	s_addc_u32 s25, s25, 0
	s_mov_b32 m0, s34
	v_lshl_add_u64 v[56:57], s[24:25], 0, v[142:143]
	ds_read_b128 v[184:187], v166 offset:32768
	ds_read_b128 v[188:191], v166 offset:33792
	ds_read_b128 v[192:195], v166 offset:34816
	ds_read_b128 v[204:207], v166 offset:35840
	ds_read_b128 v[208:211], v166 offset:36864
	ds_read_b128 v[212:215], v166 offset:37888
	ds_read_b128 v[216:219], v166 offset:38912
	ds_read_b128 v[220:223], v166 offset:39936
	global_load_lds_dwordx4 v[56:57], off
	v_lshl_add_u64 v[56:57], s[24:25], 0, v[146:147]
	s_mov_b32 m0, s35
	s_nop 0
	global_load_lds_dwordx4 v[56:57], off
	s_waitcnt vmcnt(8)
	s_waitcnt lgkmcnt(0)
	s_barrier
	s_setprio 1
	s_waitcnt lgkmcnt(0)
	v_mfma_f32_16x16x32_bf16 v[138:141], v[62:65], v[184:187], v[138:141]
	v_mfma_f32_16x16x32_bf16 v[134:137], v[156:159], v[184:187], v[134:137]
	v_mfma_f32_16x16x32_bf16 v[122:125], v[62:65], v[192:195], v[122:125]
	v_mfma_f32_16x16x32_bf16 v[118:121], v[156:159], v[192:195], v[118:121]
	v_mfma_f32_16x16x32_bf16 v[106:109], v[62:65], v[208:211], v[106:109]
	v_mfma_f32_16x16x32_bf16 v[102:105], v[156:159], v[208:211], v[102:105]
	v_mfma_f32_16x16x32_bf16 v[90:93], v[62:65], v[216:219], v[90:93]
	v_mfma_f32_16x16x32_bf16 v[86:89], v[156:159], v[216:219], v[86:89]
	v_mfma_f32_16x16x32_bf16 v[138:141], v[66:69], v[188:191], v[138:141]
	v_mfma_f32_16x16x32_bf16 v[134:137], v[160:163], v[188:191], v[134:137]
	v_mfma_f32_16x16x32_bf16 v[122:125], v[66:69], v[204:207], v[122:125]
	v_mfma_f32_16x16x32_bf16 v[118:121], v[160:163], v[204:207], v[118:121]
	v_mfma_f32_16x16x32_bf16 v[106:109], v[66:69], v[212:215], v[106:109]
	v_mfma_f32_16x16x32_bf16 v[102:105], v[160:163], v[212:215], v[102:105]
	v_mfma_f32_16x16x32_bf16 v[90:93], v[66:69], v[220:223], v[90:93]
	v_mfma_f32_16x16x32_bf16 v[86:89], v[160:163], v[220:223], v[86:89]
	s_setprio 0
	s_setprio 1
	v_mfma_f32_16x16x32_bf16 v[130:133], v[168:171], v[184:187], v[130:133]
	v_mfma_f32_16x16x32_bf16 v[126:129], v[176:179], v[184:187], v[126:129]
	v_mfma_f32_16x16x32_bf16 v[114:117], v[168:171], v[192:195], v[114:117]
	v_mfma_f32_16x16x32_bf16 v[110:113], v[176:179], v[192:195], v[110:113]
	v_mfma_f32_16x16x32_bf16 v[98:101], v[168:171], v[208:211], v[98:101]
	v_mfma_f32_16x16x32_bf16 v[94:97], v[176:179], v[208:211], v[94:97]
	v_mfma_f32_16x16x32_bf16 v[82:85], v[168:171], v[216:219], v[82:85]
	v_mfma_f32_16x16x32_bf16 v[78:81], v[176:179], v[216:219], v[78:81]
	v_mfma_f32_16x16x32_bf16 v[130:133], v[172:175], v[188:191], v[130:133]
	v_mfma_f32_16x16x32_bf16 v[126:129], v[180:183], v[188:191], v[126:129]
	v_mfma_f32_16x16x32_bf16 v[114:117], v[172:175], v[204:207], v[114:117]
	v_mfma_f32_16x16x32_bf16 v[110:113], v[180:183], v[204:207], v[110:113]
	s_barrier
; #define PG8_STAGE(bufoff, gbase, voff) do { _Pragma("unroll") for (int _i = 0; _i < 2; ++_i) \
;         __builtin_amdgcn_global_load_lds((const unsigned*)((const char*)(gbase) + (voff)[_i]), (LAS unsigned*)(lds + (bufoff) + ldsw + _i * 8192), 16, 0, 0); } while (0)
; #define PG8_LDA(dst, b, h) do { _Pragma("unroll") for (int m = 0; m < 4; ++m) _Pragma("unroll") for (int k = 0; k < 2; ++k) dst[m][k] = *(const LAS bf16x8*)(lds + PG8_SA(b, h) + aoff + m * 2048 + k * 1024); } while (0)
; #define PG8_MMA(ai, bj, At, Bt) do { __builtin_amdgcn_s_setprio(1); _Pragma("unroll") for (int m = 0; m < 4; ++m) _Pragma("unroll") for (int n = 0; n < 2; ++n) _Pragma("unroll") for (int k = 0; k < 2; ++k) \
;         acc[ai][bj][m][n] = __builtin_amdgcn_mfma_f32_16x16x32_bf16(Bt[n][k], At[m][k], acc[ai][bj][m][n], 0, 0, 0); __builtin_amdgcn_s_setprio(0); } while (0)
; #define PG8_WAIT_V(n) asm volatile("s_waitcnt vmcnt(" #n ")" ::: "memory")
; #define PG8_WAIT_L(n) asm volatile("s_waitcnt lgkmcnt(" #n ")" ::: "memory")
; #define PG8_BAR __builtin_amdgcn_s_barrier()
; #define PG8_SCHED __builtin_amdgcn_sched_barrier(0)
; #define PG8_STAGE(bufoff, gbase, voff) do { _Pragma("unroll") for (int _i = 0; _i < 2; ++_i) \
;         __builtin_amdgcn_global_load_lds((const unsigned*)((const char*)(gbase) + (voff)[_i]), (LAS unsigned*)(lds + (bufoff) + ldsw + _i * 8192), 16, 0, 0); } while (0)
; #define PG8_LDA(dst, b, h) do { _Pragma("unroll") for (int m = 0; m < 4; ++m) _Pragma("unroll") for (int k = 0; k < 2; ++k) dst[m][k] = *(const LAS bf16x8*)(lds + PG8_SA(b, h) + aoff + m * 2048 + k * 1024); } while (0)
; #define PG8_MMA(ai, bj, At, Bt) do { __builtin_amdgcn_s_setprio(1); _Pragma("unroll") for (int m = 0; m < 4; ++m) _Pragma("unroll") for (int n = 0; n < 2; ++n) _Pragma("unroll") for (int k = 0; k < 2; ++k) \
;         acc[ai][bj][m][n] = __builtin_amdgcn_mfma_f32_16x16x32_bf16(Bt[n][k], At[m][k], acc[ai][bj][m][n], 0, 0, 0); __builtin_amdgcn_s_setprio(0); } while (0)
;     ...
;             PG8_WAIT_V(8); PG8_WAIT_L(0); PG8_BAR; PG8_MMA(0, 0, At, B0); PG8_MMA(0, 1, At, B1); PG8_BAR; PG8_SCHED;
;             PG8_LDA(At, 1, 1); PG8_STAGE(PG8_SB(1, 0), b3, voffB); PG8_STAGE(PG8_SB(1, 1), b3 + hstep, voffB); PG8_STAGE(PG8_SA(1, 0), a3, voffA);
;             PG8_WAIT_V(8); PG8_WAIT_L(0); PG8_BAR; if (hi_on) { PG8_MMA(1, 0, At, B0); PG8_MMA(1, 1, At, B1); } PG8_BAR; PG8_SCHED;
;         }
	v_mfma_f32_16x16x32_bf16 v[98:101], v[172:175], v[212:215], v[98:101]
	v_mfma_f32_16x16x32_bf16 v[94:97], v[180:183], v[212:215], v[94:97]
	v_mfma_f32_16x16x32_bf16 v[82:85], v[172:175], v[220:223], v[82:85]
	v_mfma_f32_16x16x32_bf16 v[78:81], v[180:183], v[220:223], v[78:81]
	s_setprio 0
	s_add_i32 s24, s27, s29
	v_lshl_add_u64 v[56:57], v[196:197], 0, s[88:89]
	s_mov_b32 m0, s24
	ds_read_b128 v[184:187], v166 offset:49152
	ds_read_b128 v[188:191], v166 offset:50176
	ds_read_b128 v[192:195], v166 offset:51200
	ds_read_b128 v[204:207], v166 offset:52224
	ds_read_b128 v[208:211], v166 offset:53248
	ds_read_b128 v[212:215], v166 offset:54272
	ds_read_b128 v[216:219], v166 offset:55296
	ds_read_b128 v[220:223], v166 offset:56320
	global_load_lds_dwordx4 v[56:57], off
	s_add_i32 m0, s24, 0x2000
	s_add_u32 s22, s22, 0x40080
	v_lshl_add_u64 v[56:57], v[224:225], 0, s[88:89]
	s_addc_u32 s23, s23, 0
	s_add_i32 s24, s36, s29
	global_load_lds_dwordx4 v[56:57], off
	v_lshl_add_u64 v[56:57], s[22:23], 0, v[144:145]
	s_mov_b32 m0, s24
	s_nop 0
	global_load_lds_dwordx4 v[56:57], off
	v_lshl_add_u64 v[56:57], s[22:23], 0, v[148:149]
	s_add_i32 m0, s24, 0x2000
	s_nop 0
	global_load_lds_dwordx4 v[56:57], off
	v_lshl_add_u64 v[56:57], v[226:227], 0, s[88:89]
	s_mov_b32 m0, s39
	s_nop 0
	global_load_lds_dwordx4 v[56:57], off
	v_lshl_add_u64 v[56:57], v[228:229], 0, s[88:89]
	s_mov_b32 m0, s40
	s_nop 0
	global_load_lds_dwordx4 v[56:57], off
	s_waitcnt vmcnt(8)
	s_waitcnt lgkmcnt(0)
	s_barrier
	s_setprio 1
	s_waitcnt lgkmcnt(0)
	v_mfma_f32_16x16x32_bf16 v[74:77], v[62:65], v[184:187], v[74:77]
	v_mfma_f32_16x16x32_bf16 v[70:73], v[156:159], v[184:187], v[70:73]
	v_mfma_f32_16x16x32_bf16 v[48:51], v[62:65], v[192:195], v[48:51]
	v_mfma_f32_16x16x32_bf16 v[44:47], v[156:159], v[192:195], v[44:47]
	v_mfma_f32_16x16x32_bf16 v[30:33], v[62:65], v[208:211], v[30:33]
	v_mfma_f32_16x16x32_bf16 v[26:29], v[156:159], v[208:211], v[26:29]
	v_mfma_f32_16x16x32_bf16 v[14:17], v[62:65], v[216:219], v[14:17]
	v_mfma_f32_16x16x32_bf16 v[10:13], v[156:159], v[216:219], v[10:13]
	v_mfma_f32_16x16x32_bf16 v[74:77], v[66:69], v[188:191], v[74:77]
	v_mfma_f32_16x16x32_bf16 v[70:73], v[160:163], v[188:191], v[70:73]
	v_mfma_f32_16x16x32_bf16 v[48:51], v[66:69], v[204:207], v[48:51]
	v_mfma_f32_16x16x32_bf16 v[44:47], v[160:163], v[204:207], v[44:47]
	v_mfma_f32_16x16x32_bf16 v[30:33], v[66:69], v[212:215], v[30:33]
	v_mfma_f32_16x16x32_bf16 v[26:29], v[160:163], v[212:215], v[26:29]
	v_mfma_f32_16x16x32_bf16 v[14:17], v[66:69], v[220:223], v[14:17]
	v_mfma_f32_16x16x32_bf16 v[10:13], v[160:163], v[220:223], v[10:13]
	s_setprio 0
	s_setprio 1
	v_mfma_f32_16x16x32_bf16 v[56:59], v[168:171], v[184:187], v[58:61]
	v_mfma_f32_16x16x32_bf16 v[52:55], v[176:179], v[184:187], v[52:55]
	v_mfma_f32_16x16x32_bf16 v[40:43], v[168:171], v[192:195], v[40:43]
	v_mfma_f32_16x16x32_bf16 v[36:39], v[176:179], v[192:195], v[36:39]
	v_mfma_f32_16x16x32_bf16 v[22:25], v[168:171], v[208:211], v[22:25]
	v_mfma_f32_16x16x32_bf16 v[18:21], v[176:179], v[208:211], v[18:21]
	v_mfma_f32_16x16x32_bf16 v[6:9], v[168:171], v[216:219], v[6:9]
	v_mfma_f32_16x16x32_bf16 v[2:5], v[176:179], v[216:219], v[2:5]
	v_mfma_f32_16x16x32_bf16 v[58:61], v[172:175], v[188:191], v[56:59]
	v_mfma_f32_16x16x32_bf16 v[54:57], v[180:183], v[188:191], v[52:55]
	v_mfma_f32_16x16x32_bf16 v[40:43], v[172:175], v[204:207], v[40:43]
	v_mfma_f32_16x16x32_bf16 v[36:39], v[180:183], v[204:207], v[36:39]
	s_barrier
	v_mfma_f32_16x16x32_bf16 v[22:25], v[172:175], v[212:215], v[22:25]
	v_mfma_f32_16x16x32_bf16 v[18:21], v[180:183], v[212:215], v[18:21]
	v_mfma_f32_16x16x32_bf16 v[6:9], v[172:175], v[220:223], v[6:9]
	v_mfma_f32_16x16x32_bf16 v[2:5], v[180:183], v[220:223], v[2:5]
	s_setprio 0
	s_add_i32 s26, s26, 2
	s_add_u32 s6, s6, 0x100
	s_addc_u32 s7, s7, 0
	s_add_u32 s15, s15, 0x100
	s_addc_u32 s17, s17, 0
	s_cmp_gt_u32 s26, 13
	s_cbranch_scc0 .LBB0_213
	s_and_b64 vcc, exec, s[12:13]
	s_cbranch_vccz .LBB0_216
	s_barrier
